# s10
# speedup vs baseline: 1.0256x; 1.0178x over previous
_Z11prep_kernelPKfS0_PKiS2_S0_S0_S0_S0_S0_S0_Pc:
	s_lshr_b32 s4, s2, 2
	v_lshrrev_b32_e32 v2, 6, v0
	s_and_b32 s4, s4, 0x1ffffffe
	s_load_dwordx4 s[28:31], s[0:1], 0x40
	s_load_dwordx8 s[12:19], s[0:1], 0x0
	s_load_dwordx8 s[20:27], s[0:1], 0x20
	v_and_b32_e32 v1, 15, v0
	s_and_b32 s3, s2, 7
	v_or_b32_e32 v2, s4, v2
	v_lshl_or_b32 v88, v2, 3, s3
	v_cmp_gt_u32_e64 s[10:11], 14, v1
	v_mul_lo_u32 v7, v88, 14
	v_and_b32_e32 v105, 63, v0
	v_cndmask_b32_e64 v6, 13, v1, s[10:11]
	v_add_u32_e32 v2, v7, v6
	s_waitcnt lgkmcnt(0)
	v_mad_i64_i32 v[4:5], s[4:5], v2, 12, s[12:13]
	global_load_dwordx3 v[82:84], v[4:5], off
	v_lshlrev_b32_e32 v4, 2, v6
	v_cmp_gt_u32_e64 s[8:9], 48, v105
	global_load_dword v85, v4, s[26:27]
	v_cmp_gt_u32_e64 s[6:7], 14, v105
	v_cndmask_b32_e64 v4, 0, v105, s[8:9]
	v_mad_u64_u32 v[4:5], s[4:5], v88, 48, v[4:5]
	v_ashrrev_i32_e32 v5, 31, v4
	v_lshl_add_u64 v[4:5], v[4:5], 2, s[18:19]
	global_load_dword v114, v[4:5], off
	v_cndmask_b32_e64 v4, 0, v105, s[6:7]
	v_add_u32_e32 v4, v7, v4
	v_lshlrev_b32_e32 v118, 1, v0
	v_ashrrev_i32_e32 v5, 31, v4
	s_lshl_b32 s2, s2, 3
	v_lshl_add_u64 v[4:5], v[4:5], 2, s[16:17]
	s_and_b32 s2, s2, 0x78
	v_lshrrev_b32_e32 v104, 4, v0
	v_and_b32_e32 v106, 30, v118
	global_load_dword v115, v[4:5], off
	v_or_b32_e32 v107, s2, v104
	v_lshlrev_b32_e32 v4, 7, v106
	v_cmp_gt_u32_e64 s[2:3], 23, v106
	v_or_b32_e32 v5, 1, v106
	v_lshlrev_b32_e32 v6, 7, v5
	v_cndmask_b32_e64 v4, 0, v4, s[2:3]
	v_cmp_gt_u32_e64 s[4:5], 23, v5
	v_or_b32_e32 v4, v4, v107
	v_lshlrev_b32_e32 v4, 2, v4
	v_cndmask_b32_e64 v5, 0, v6, s[4:5]
	v_or_b32_e32 v5, v5, v107
	v_lshlrev_b32_e32 v5, 2, v5
	global_load_dword v116, v4, s[28:29]
	global_load_dword v113, v5, s[28:29]
	v_lshlrev_b32_e32 v4, 2, v107
	s_movk_i32 s12, 0x100
	global_load_dword v117, v4, s[30:31]
	v_lshlrev_b32_e32 v4, 2, v0
	v_mov_b32_e32 v8, s25
	v_mov_b32_e32 v9, s21
	v_cmp_gt_u32_e32 vcc, s12, v0
	v_mov_b32_e32 v10, s24
	v_mov_b32_e32 v11, s20
	v_lshlrev_b32_e32 v119, 5, v0
	v_and_b32_e32 v109, 12, v4
	v_cndmask_b32_e32 v5, v8, v9, vcc
	v_cndmask_b32_e32 v4, v10, v11, vcc
	v_and_b32_e32 v86, 0xf80, v119
	v_mov_b32_e32 v87, 0
	v_lshl_add_u64 v[4:5], v[4:5], 0, v[86:87]
	v_lshlrev_b32_e32 v6, 2, v109
	v_mov_b32_e32 v7, v87
	s_movk_i32 s12, 0x80
	v_lshl_add_u64 v[4:5], v[4:5], 0, v[6:7]
	v_or_b32_e32 v112, 0x80, v0
	v_cmp_gt_u32_e32 vcc, s12, v0
	global_load_dwordx4 v[66:69], v[4:5], off
	global_load_dwordx4 v[70:73], v[4:5], off offset:64
	v_cndmask_b32_e32 v5, v8, v9, vcc
	v_lshlrev_b32_e32 v8, 5, v112
	v_cndmask_b32_e32 v4, v10, v11, vcc
	v_and_b32_e32 v8, 0x1f80, v8
	v_mov_b32_e32 v9, v87
	v_lshl_add_u64 v[4:5], v[4:5], 0, v[8:9]
	v_lshl_add_u64 v[4:5], v[4:5], 0, v[6:7]
	global_load_dwordx4 v[74:77], v[4:5], off
	global_load_dwordx4 v[78:81], v[4:5], off offset:64
	v_lshl_add_u64 v[4:5], s[22:23], 0, v[86:87]
	v_lshl_add_u64 v[4:5], v[4:5], 0, v[6:7]
	v_or_b32_e32 v111, 0x180, v0
	global_load_dwordx4 v[58:61], v[4:5], off
	global_load_dwordx4 v[62:65], v[4:5], off offset:64
	v_lshlrev_b32_e32 v4, 5, v111
	v_and_b32_e32 v4, 0x1f80, v4
	v_mov_b32_e32 v5, v87
	v_lshl_add_u64 v[4:5], s[22:23], 0, v[4:5]
	v_lshl_add_u64 v[4:5], v[4:5], 0, v[6:7]
	global_load_dwordx4 v[50:53], v[4:5], off
	global_load_dwordx4 v[54:57], v[4:5], off offset:64
	v_lshl_add_u64 v[4:5], s[24:25], 0, v[86:87]
	v_lshl_add_u64 v[4:5], v[4:5], 0, v[6:7]
	v_or_b32_e32 v108, 0x280, v0
	global_load_dwordx4 v[42:45], v[4:5], off
	global_load_dwordx4 v[46:49], v[4:5], off offset:64
	v_lshlrev_b32_e32 v4, 5, v108
	v_and_b32_e32 v86, 0x1f80, v4
	v_ashrrev_i32_e32 v3, 31, v2
	v_lshl_add_u64 v[4:5], s[24:25], 0, v[86:87]
	v_lshl_add_u64 v[4:5], v[4:5], 0, v[6:7]
	v_lshlrev_b64 v[2:3], 9, v[2:3]
	global_load_dwordx4 v[34:37], v[4:5], off
	global_load_dwordx4 v[38:41], v[4:5], off offset:64
	v_lshl_add_u64 v[2:3], s[14:15], 0, v[2:3]
	v_and_b32_e32 v4, 48, v0
	v_mov_b32_e32 v5, v87
	v_lshl_add_u64 v[90:91], v[2:3], 0, v[4:5]
	global_load_dwordx4 v[26:29], v[90:91], off nt
	global_load_dwordx4 v[30:33], v[90:91], off offset:64 nt
	global_load_dwordx4 v[18:21], v[90:91], off offset:128 nt
	global_load_dwordx4 v[22:25], v[90:91], off offset:192 nt
	global_load_dwordx4 v[10:13], v[90:91], off offset:256 nt
	global_load_dwordx4 v[14:17], v[90:91], off offset:320 nt
	global_load_dwordx4 v[2:5], v[90:91], off offset:384 nt
	global_load_dwordx4 v[6:9], v[90:91], off offset:448 nt
	v_bfe_u32 v110, v0, 4, 2
	s_waitcnt vmcnt(26)
	v_mov_b32_e32 v90, v83
	v_mov_b32_e32 v91, v84
	v_lshlrev_b32_e32 v86, 2, v110
	s_waitcnt vmcnt(25)
	v_mul_f32_e32 v84, 0x3fb8aa3b, v85
	s_mov_b32 s14, 0x41700000
	v_exp_f32_e32 v84, v84
	v_cndmask_b32_e64 v94, 0, 1.0, s[10:11]
	v_add_f32_e32 v84, 1.0, v84
	v_cmp_lt_f32_e32 vcc, s14, v85
	v_log_f32_e32 v84, v84
	v_cmp_lt_u32_e64 s[12:13], 15, v105
	v_mul_f32_e32 v84, 0x3f317218, v84
	v_cndmask_b32_e32 v84, v84, v85, vcc
	v_mul_f32_e32 v84, 0xbe715bef, v84
	v_mul_f32_e32 v84, 0x3f3504f3, v84
	v_mul_f32_e32 v84, 0x41800000, v84
	v_cndmask_b32_e64 v99, 0, v84, s[10:11]
	v_mul_f32_e32 v101, -2.0, v99
	v_mov_b32_e32 v95, v101
	v_pk_mul_f32 v[84:85], v[94:95], v[82:83] op_sel:[0,1]
	v_cmp_gt_u32_e32 vcc, 16, v105
	v_mov_b32_e32 v83, v85
	s_and_saveexec_b64 s[14:15], s[12:13]
	s_xor_b64 s[14:15], exec, s[14:15]
	s_cbranch_execz .LBB0_10
	v_pk_mul_f32 v[92:93], v[90:91], v[90:91]
	v_mov_b32_e32 v95, v91
	v_fma_f32 v83, v82, v82, v92
	v_add_f32_e32 v100, v83, v93
	v_pk_mul_f32 v[92:93], v[94:95], v[100:101]
	v_mov_b32_e32 v83, v87
	v_cvt_pk_fp8_f32 v83, v93, 0
	v_mul_f32_e32 v98, v94, v91
	v_cmp_lt_i32_e64 s[12:13], 1, v110
	s_mov_b64 s[16:17], 0
	v_cvt_f32_fp8_e32 v83, v83
	v_sub_f32_e32 v89, v93, v83
	s_and_saveexec_b64 s[18:19], s[12:13]
	s_xor_b64 s[18:19], exec, s[18:19]
	s_cbranch_execz .LBB0_5
	v_cmp_eq_u32_e64 s[12:13], 2, v110
	s_mov_b64 s[20:21], -1
	s_and_saveexec_b64 s[16:17], s[12:13]
	s_cbranch_execz .LBB0_4
	v_mov_b32_e32 v83, 0
	v_mov_b32_e32 v84, 0
	v_mov_b32_e32 v89, 0
	v_cvt_pk_fp8_f32 v84, v99, 0
	v_cvt_pk_fp8_f32 v89, v98, 0
	v_cvt_pk_fp8_f32 v83, v92, 0
	s_xor_b64 s[20:21], exec, -1
	v_cvt_f32_fp8_e32 v85, v84
	v_cvt_f32_fp8_e32 v84, v89
	v_cvt_f32_fp8_e32 v83, v83
	v_mov_b32_e32 v102, v92
	v_pk_add_f32 v[96:97], v[98:99], v[84:85] neg_lo:[0,1] neg_hi:[0,1]
	v_sub_f32_e32 v84, v92, v83

.LBB0_18:
	s_or_b64 exec, exec, s[6:7]
	s_waitcnt vmcnt(22)
	v_cvt_f16_f32_e32 v89, v117
	v_cvt_f16_f32_e32 v88, v116
	v_cvt_f16_f32_e32 v90, v113
	v_cmp_eq_u32_e32 vcc, 22, v106
	s_mov_b32 s0, 0x160000
	v_cndmask_b32_e64 v88, 0, v88, s[2:3]
	v_cndmask_b32_e32 v89, 0, v89, vcc
	v_cndmask_b32_e64 v89, v89, v90, s[4:5]
	v_pack_b32_f16 v96, v88, v89
	v_lshlrev_b32_e32 v88, 6, v107
	v_mov_b32_e32 v89, 0
	v_lshl_add_u64 v[90:91], s[12:13], 0, v[88:89]
	v_lshlrev_b32_e32 v88, 1, v106
	v_lshl_add_u64 v[90:91], v[90:91], 0, v[88:89]
	v_add_co_u32_e32 v90, vcc, s0, v90
	s_nop 1
	v_addc_co_u32_e32 v91, vcc, 0, v91, vcc
	global_store_dword v[90:91], v96, off
	v_lshrrev_b32_e32 v88, 1, v0
	v_and_b32_e32 v90, 24, v0
	v_lshrrev_b32_e32 v0, 3, v0
	v_and_b32_e32 v0, 4, v0
	v_and_b32_e32 v91, 2, v88
	v_or3_b32 v0, v0, v90, v91
	s_movk_i32 s1, 0x60
	v_and_or_b32 v88, v88, s1, v0
	s_waitcnt vmcnt(21)
	v_cvt_pk_f16_f32 v66, v66, v70
	v_and_b32_e32 v70, 48, v104
	v_mul_u32_u24_e32 v90, 0x110, v109
	v_mul_u32_u24_e32 v70, 0x110, v70
	v_lshlrev_b32_e32 v88, 1, v88
	v_add3_u32 v70, v90, v70, v88
	v_cvt_pk_f16_f32 v67, v67, v71
	ds_write2_b32 v70, v66, v67 offset1:68
	v_cvt_pk_f16_f32 v66, v68, v72
	v_cvt_pk_f16_f32 v67, v69, v73
	ds_write2_b32 v70, v66, v67 offset0:136 offset1:204
	v_lshrrev_b32_e32 v66, 1, v112
	v_lshrrev_b32_e32 v68, 4, v112
	v_and_or_b32 v66, v66, s1, v0
	v_and_b32_e32 v68, 0x70, v68
	s_waitcnt vmcnt(17)
	v_cvt_pk_f16_f32 v58, v58, v62
	v_lshrrev_b32_e32 v62, 4, v95
	v_mul_u32_u24_e32 v68, 0x110, v68
	v_lshlrev_b32_e32 v66, 1, v66
	v_and_b32_e32 v62, 0x70, v62
	v_cvt_pk_f16_f32 v67, v74, v78
	v_add3_u32 v66, v90, v68, v66
	v_cvt_pk_f16_f32 v68, v75, v79
	v_mul_u32_u24_e32 v62, 0x110, v62
	ds_write2_b32 v66, v67, v68 offset1:68
	v_cvt_pk_f16_f32 v67, v76, v80
	v_cvt_pk_f16_f32 v68, v77, v81
	v_add3_u32 v62, v90, v62, v88
	v_cvt_pk_f16_f32 v59, v59, v63
	ds_write2_b32 v66, v67, v68 offset0:136 offset1:204
	ds_write2_b32 v62, v58, v59 offset1:68
	v_cvt_pk_f16_f32 v58, v60, v64
	v_cvt_pk_f16_f32 v59, v61, v65
	ds_write2_b32 v62, v58, v59 offset0:136 offset1:204
	v_lshrrev_b32_e32 v58, 1, v111
	s_waitcnt vmcnt(15)
	v_cvt_pk_f16_f32 v50, v50, v54
	v_lshrrev_b32_e32 v54, 4, v111
	v_and_or_b32 v58, v58, s1, v0
	v_and_b32_e32 v54, 0x70, v54
	s_waitcnt vmcnt(13)
	v_cvt_pk_f16_f32 v42, v42, v46
	v_lshrrev_b32_e32 v46, 4, v94
	v_mul_u32_u24_e32 v54, 0x110, v54
	v_lshlrev_b32_e32 v58, 1, v58
	v_and_b32_e32 v46, 0x70, v46
	v_add3_u32 v54, v90, v54, v58
	v_cvt_pk_f16_f32 v51, v51, v55
	v_mul_u32_u24_e32 v46, 0x110, v46
	ds_write2_b32 v54, v50, v51 offset1:68
	v_cvt_pk_f16_f32 v50, v52, v56
	v_cvt_pk_f16_f32 v51, v53, v57
	v_add3_u32 v46, v90, v46, v88
	v_cvt_pk_f16_f32 v43, v43, v47
	ds_write2_b32 v54, v50, v51 offset0:136 offset1:204
	ds_write2_b32 v46, v42, v43 offset1:68
	v_cvt_pk_f16_f32 v42, v44, v48
	v_cvt_pk_f16_f32 v43, v45, v49
	ds_write2_b32 v46, v42, v43 offset0:136 offset1:204
	v_lshrrev_b32_e32 v42, 1, v108
	s_waitcnt vmcnt(11)
	v_cvt_pk_f16_f32 v34, v34, v38
	v_lshrrev_b32_e32 v38, 4, v108
	v_and_or_b32 v0, v42, s1, v0
	v_and_b32_e32 v38, 0x70, v38
	v_mul_u32_u24_e32 v38, 0x110, v38
	v_lshlrev_b32_e32 v0, 1, v0
	v_add3_u32 v0, v90, v38, v0
	v_cvt_pk_f16_f32 v35, v35, v39
	ds_write2_b32 v0, v34, v35 offset1:68
	v_cvt_pk_f16_f32 v34, v36, v40
	v_cvt_pk_f16_f32 v35, v37, v41
	s_movk_i32 s0, 0x110
	ds_write2_b32 v0, v34, v35 offset0:136 offset1:204
	s_waitcnt vmcnt(9)
	v_cvt_pk_f16_f32 v39, v32, v33
	v_lshlrev_b32_e32 v32, 4, v110
	v_mad_u32_u24 v48, v1, s0, v32
	s_waitcnt lgkmcnt(0)
	s_barrier
	ds_read_b128 v[32:35], v48
	v_cvt_pk_f16_f32 v38, v30, v31
	v_cvt_pk_f16_f32 v37, v28, v29
	v_cvt_pk_f16_f32 v36, v26, v27
	ds_read_b128 v[26:29], v48 offset:64
	s_waitcnt vmcnt(7)
	v_cvt_pk_f16_f32 v25, v24, v25
	s_waitcnt lgkmcnt(1)
	v_mfma_f32_16x16x32_f16 v[124:127], v[32:35], v[36:39], 0
	ds_read_b128 v[30:33], v48 offset:4352
	ds_read_b128 v[40:43], v48 offset:4416
	v_cvt_pk_f16_f32 v24, v22, v23
	s_waitcnt lgkmcnt(1)
	v_mfma_f32_16x16x32_f16 v[128:131], v[30:33], v[36:39], 0
	ds_read_b128 v[30:33], v48 offset:8704
	ds_read_b128 v[44:47], v48 offset:8768
	v_cvt_pk_f16_f32 v23, v20, v21
	v_cvt_pk_f16_f32 v22, v18, v19
	s_waitcnt lgkmcnt(1)
	v_mfma_f32_16x16x32_f16 v[132:135], v[36:39], v[30:33], 0
	s_waitcnt vmcnt(5)
	v_cvt_pk_f16_f32 v0, v16, v17
	ds_read_b128 v[16:19], v48 offset:128
	v_lshlrev_b32_e32 v88, 4, v1
	v_mfma_f32_16x16x32_f16 v[124:127], v[26:29], v[22:25], v[124:127]
	v_mfma_f32_16x16x32_f16 v[128:131], v[40:43], v[22:25], v[128:131]
	s_waitcnt lgkmcnt(1)
	v_mfma_f32_16x16x32_f16 v[132:135], v[22:25], v[44:47], v[132:135]
	v_cndmask_b32_e64 v23, 0, v0, s[10:11]
	v_cvt_pk_f16_f32 v22, v14, v15
	v_cvt_pk_f16_f32 v21, v12, v13
	v_cvt_pk_f16_f32 v20, v10, v11
	ds_read_b128 v[10:13], v48 offset:192
	s_waitcnt vmcnt(3)
	v_cvt_pk_f16_f32 v9, v8, v9
	s_waitcnt lgkmcnt(1)
	v_mfma_f32_16x16x32_f16 v[124:127], v[16:19], v[20:23], v[124:127]
	v_cvt_pk_f16_f32 v8, v6, v7
	v_cvt_pk_f16_f32 v7, v4, v5
	ds_read_b128 v[14:17], v48 offset:4480
	ds_read_b128 v[24:27], v48 offset:4544
	v_cvt_pk_f16_f32 v6, v2, v3
	s_waitcnt lgkmcnt(1)
	v_mfma_f32_16x16x32_f16 v[128:131], v[14:17], v[20:23], v[128:131]
	ds_read_b128 v[14:17], v48 offset:8832
	ds_read_b128 v[28:31], v48 offset:8896
	v_mfma_f32_16x16x32_f16 v[124:127], v[10:13], v[6:9], v[124:127]
	s_waitcnt lgkmcnt(2)
	v_mfma_f32_16x16x32_f16 v[128:131], v[24:27], v[6:9], v[128:131]
	s_waitcnt lgkmcnt(1)
	v_mfma_f32_16x16x32_f16 v[132:135], v[20:23], v[14:17], v[132:135]
	s_waitcnt lgkmcnt(0)
	v_mfma_f32_16x16x32_f16 v[132:135], v[6:9], v[28:31], v[132:135]
	s_nop 2
	v_mul_f32_e32 v96, 0x403504f3, v124
	v_mul_f32_e32 v97, 0x403504f3, v125
	v_mul_f32_e32 v98, 0x403504f3, v126
	v_mul_f32_e32 v99, 0x403504f3, v127
	v_cvt_pk_fp8_f32 v100, v96, v97
	v_cvt_pk_fp8_f32 v100, v98, v99 op_sel:[0,0,1]
	v_mul_f32_e32 v96, 4.0, v128
	v_mul_f32_e32 v97, 4.0, v129
	v_mul_f32_e32 v98, 4.0, v130
	v_mul_f32_e32 v99, 4.0, v131
	v_cvt_pk_fp8_f32 v101, v96, v97
	v_cvt_pk_fp8_f32 v101, v98, v99 op_sel:[0,0,1]
	global_store_dword v[92:93], v100, off
	global_store_dword v[84:85], v101, off
	v_mul_f32_e32 v96, 4.0, v132
	v_mul_f32_e32 v97, 4.0, v133
	v_mul_f32_e32 v98, 4.0, v134
	v_mul_f32_e32 v99, 4.0, v135
	v_lshl_add_u64 v[0:1], v[82:83], 0, v[88:89]
	v_cvt_pk_fp8_f32 v102, v96, v97
	v_lshl_add_u64 v[0:1], v[0:1], 0, v[86:87]
	v_cvt_pk_fp8_f32 v102, v98, v99 op_sel:[0,0,1]
	v_add_co_u32_e32 v0, vcc, 0x100000, v0
	s_nop 1
	v_addc_co_u32_e32 v1, vcc, 0, v1, vcc
	global_store_dword v[0:1], v102, off
	s_endpgm

	.amdhsa_kernel _Z11prep_kernelPKfS0_PKiS2_S0_S0_S0_S0_S0_S0_Pc
		.amdhsa_group_segment_fixed_size 13056
		.amdhsa_private_segment_fixed_size 0
		.amdhsa_kernarg_size 88
		.amdhsa_user_sgpr_count 2
		.amdhsa_user_sgpr_dispatch_ptr 0
		.amdhsa_user_sgpr_queue_ptr 0
		.amdhsa_user_sgpr_kernarg_segment_ptr 1
		.amdhsa_user_sgpr_dispatch_id 0
		.amdhsa_user_sgpr_kernarg_preload_length 0
		.amdhsa_user_sgpr_kernarg_preload_offset 0
		.amdhsa_user_sgpr_private_segment_size 0
		.amdhsa_uses_dynamic_stack 0
		.amdhsa_enable_private_segment 0
		.amdhsa_system_sgpr_workgroup_id_x 1
		.amdhsa_system_sgpr_workgroup_id_y 0
		.amdhsa_system_sgpr_workgroup_id_z 0
		.amdhsa_system_sgpr_workgroup_info 0
		.amdhsa_system_vgpr_workitem_id 0
		.amdhsa_next_free_vgpr 136
		.amdhsa_next_free_sgpr 91
		.amdhsa_accum_offset 136
		.amdhsa_reserve_vcc 1
		.amdhsa_float_round_mode_32 0
		.amdhsa_float_round_mode_16_64 0
		.amdhsa_float_denorm_mode_32 3
		.amdhsa_float_denorm_mode_16_64 3
		.amdhsa_dx10_clamp 1
		.amdhsa_ieee_mode 1
		.amdhsa_fp16_overflow 0
		.amdhsa_tg_split 0
		.amdhsa_exception_fp_ieee_invalid_op 0
		.amdhsa_exception_fp_denorm_src 0
		.amdhsa_exception_fp_ieee_div_zero 0
		.amdhsa_exception_fp_ieee_overflow 0
		.amdhsa_exception_fp_ieee_underflow 0
		.amdhsa_exception_fp_ieee_inexact 0
		.amdhsa_exception_int_div_zero 0
	.end_amdhsa_kernel

.LBB1_41:
	s_or_b64 exec, exec, s[0:1]
	v_mul_u32_u24_e32 v18, 0x50, v57
	v_lshl_add_u32 v18, v58, 1, v18
	v_lshlrev_b32_e32 v23, 2, v57
	v_and_b32_e32 v22, 0xc0, v0
	v_lshlrev_b32_e32 v25, 11, v1
	v_or3_b32 v25, v23, v22, v25
	s_waitcnt lgkmcnt(0)
	s_barrier
	ds_read_b128 v[18:21], v18 offset:14336
	s_mul_i32 s6, s2, 14
	v_bfe_u32 v41, s3, v56, 1
	v_add_u32_e32 v40, s6, v56
	v_cvt_f32_u32_e32 v41, v41
	v_lshl_add_u32 v40, v40, 9, v54
	v_lshl_or_b32 v0, v56, 9, v54
	s_waitcnt vmcnt(4) lgkmcnt(0)
	v_mfma_f32_16x16x32_f16 v[14:17], v[18:21], v[124:127], 0
	v_mfma_f32_16x16x32_f16 v[6:9], v[18:21], v[128:131], 0
	s_nop 6
	ds_write2st64_b32 v25, v14, v15 offset1:2
	ds_write2st64_b32 v25, v16, v17 offset0:4 offset1:6
	ds_write2st64_b32 v25, v6, v7 offset0:1 offset1:3
	ds_write2st64_b32 v25, v8, v9 offset0:5 offset1:7
	s_waitcnt lgkmcnt(0)
	s_barrier
	s_and_saveexec_b64 s[0:1], s[4:5]
	s_cbranch_execz .LBB1_53
	ds_read_b128 v[14:17], v0
	ds_read_b128 v[6:9], v0 offset:256
	ds_read_b128 v[24:27], v54 offset:15616
	ds_read_b128 v[28:31], v54 offset:15872
	ds_read_b128 v[32:35], v54 offset:16128
	ds_read_b128 v[36:39], v54 offset:16384
	s_waitcnt vmcnt(0) lgkmcnt(4)
	v_pk_fma_f32 v[136:137], v[14:15], v[40:41], v[136:137] op_sel:[0,1,0]
	v_pk_fma_f32 v[138:139], v[16:17], v[40:41], v[138:139] op_sel:[0,1,0]
	v_pk_fma_f32 v[140:141], v[6:7], v[40:41], v[140:141] op_sel:[0,1,0]
	v_pk_fma_f32 v[142:143], v[8:9], v[40:41], v[142:143] op_sel:[0,1,0]
	v_pk_add_f32 v[10:11], v[136:137], v[138:139]
	v_pk_add_f32 v[12:13], v[140:141], v[142:143]
	v_mov_b32_e32 v15, 0x3727c5ac
	v_pk_add_f32 v[10:11], v[10:11], v[12:13]
	s_nop 0
	v_add_f32_e32 v10, v10, v11
	s_nop 1
	v_add_f32_dpp v10, v10, v10 quad_perm:[1,0,3,2] row_mask:0xf bank_mask:0xf bound_ctrl:1
	s_nop 1
	v_add_f32_dpp v10, v10, v10 quad_perm:[2,3,0,1] row_mask:0xf bank_mask:0xf bound_ctrl:1
	s_nop 1
	v_add_f32_dpp v10, v10, v10 row_half_mirror row_mask:0xf bank_mask:0xf bound_ctrl:1
	s_nop 1
	v_add_f32_dpp v10, v10, v10 row_mirror row_mask:0xf bank_mask:0xf bound_ctrl:1
	v_mul_f32_e32 v10, 0x3c000000, v10
	v_pk_add_f32 v[136:137], v[136:137], v[10:11] op_sel_hi:[1,0] neg_lo:[0,1] neg_hi:[0,1]
	v_pk_add_f32 v[138:139], v[138:139], v[10:11] op_sel_hi:[1,0] neg_lo:[0,1] neg_hi:[0,1]
	v_pk_add_f32 v[140:141], v[140:141], v[10:11] op_sel_hi:[1,0] neg_lo:[0,1] neg_hi:[0,1]
	v_pk_add_f32 v[142:143], v[142:143], v[10:11] op_sel_hi:[1,0] neg_lo:[0,1] neg_hi:[0,1]
	v_pk_mul_f32 v[12:13], v[136:137], v[136:137]
	v_pk_mul_f32 v[16:17], v[138:139], v[138:139]
	v_pk_fma_f32 v[12:13], v[140:141], v[140:141], v[12:13]
	v_pk_fma_f32 v[16:17], v[142:143], v[142:143], v[16:17]
	s_nop 0
	v_pk_add_f32 v[12:13], v[12:13], v[16:17]
	s_nop 0
	v_add_f32_e32 v12, v12, v13
	s_nop 1
	v_add_f32_dpp v12, v12, v12 quad_perm:[1,0,3,2] row_mask:0xf bank_mask:0xf bound_ctrl:1
	s_nop 1
	v_add_f32_dpp v12, v12, v12 quad_perm:[2,3,0,1] row_mask:0xf bank_mask:0xf bound_ctrl:1
	s_nop 1
	v_add_f32_dpp v12, v12, v12 row_half_mirror row_mask:0xf bank_mask:0xf bound_ctrl:1
	s_nop 1
	v_add_f32_dpp v12, v12, v12 row_mirror row_mask:0xf bank_mask:0xf bound_ctrl:1
	v_fmac_f32_e32 v15, 0x3c000000, v12
	v_rsq_f32_e32 v14, v15
	s_nop 0
	v_pk_mul_f32 v[136:137], v[136:137], v[14:15] op_sel_hi:[1,0]
	v_pk_mul_f32 v[138:139], v[138:139], v[14:15] op_sel_hi:[1,0]
	v_pk_mul_f32 v[140:141], v[140:141], v[14:15] op_sel_hi:[1,0]
	v_pk_mul_f32 v[142:143], v[142:143], v[14:15] op_sel_hi:[1,0]
	s_waitcnt lgkmcnt(0)
	v_pk_fma_f32 v[136:137], v[24:25], v[136:137], v[32:33]
	v_pk_fma_f32 v[138:139], v[26:27], v[138:139], v[34:35]
	v_pk_fma_f32 v[140:141], v[28:29], v[140:141], v[36:37]
	v_pk_fma_f32 v[142:143], v[30:31], v[142:143], v[38:39]
	global_store_dwordx4 v40, v[136:139], s[14:15] nt
	global_store_dwordx4 v40, v[140:143], s[14:15] offset:256 nt

amdhsa.kernels:
  - .agpr_count:     0
    .args:
      - .actual_access:  read_only
        .address_space:  global
        .offset:         0
        .size:           8
        .value_kind:     global_buffer
      - .actual_access:  read_only
        .address_space:  global
        .offset:         8
        .size:           8
        .value_kind:     global_buffer
      - .actual_access:  read_only
        .address_space:  global
        .offset:         16
        .size:           8
        .value_kind:     global_buffer
      - .actual_access:  read_only
        .address_space:  global
        .offset:         24
        .size:           8
        .value_kind:     global_buffer
      - .actual_access:  read_only
        .address_space:  global
        .offset:         32
        .size:           8
        .value_kind:     global_buffer
      - .actual_access:  read_only
        .address_space:  global
        .offset:         40
        .size:           8
        .value_kind:     global_buffer
      - .actual_access:  read_only
        .address_space:  global
        .offset:         48
        .size:           8
        .value_kind:     global_buffer
      - .actual_access:  read_only
        .address_space:  global
        .offset:         56
        .size:           8
        .value_kind:     global_buffer
      - .actual_access:  read_only
        .address_space:  global
        .offset:         64
        .size:           8
        .value_kind:     global_buffer
      - .actual_access:  read_only
        .address_space:  global
        .offset:         72
        .size:           8
        .value_kind:     global_buffer
      - .actual_access:  write_only
        .address_space:  global
        .offset:         80
        .size:           8
        .value_kind:     global_buffer
    .group_segment_fixed_size: 13056
    .kernarg_segment_align: 8
    .kernarg_segment_size: 88
    .language:       OpenCL C
    .language_version:
      - 2
      - 0
    .max_flat_workgroup_size: 128
    .name:           _Z11prep_kernelPKfS0_PKiS2_S0_S0_S0_S0_S0_S0_Pc
    .private_segment_fixed_size: 0
    .sgpr_count:     38
    .sgpr_spill_count: 0
    .symbol:         _Z11prep_kernelPKfS0_PKiS2_S0_S0_S0_S0_S0_S0_Pc.kd
    .uniform_work_group_size: 1
    .uses_dynamic_stack: false
    .vgpr_count:     136
    .vgpr_spill_count: 0
    .wavefront_size: 64
  - .agpr_count:     0
    .args:
      - .actual_access:  read_only
        .address_space:  global
        .offset:         0
        .size:           8
        .value_kind:     global_buffer
      - .actual_access:  read_only
        .address_space:  global
        .offset:         8
        .size:           8
        .value_kind:     global_buffer
      - .actual_access:  read_only
        .address_space:  global
        .offset:         16
        .size:           8
        .value_kind:     global_buffer
      - .actual_access:  read_only
        .address_space:  global
        .offset:         24
        .size:           8
        .value_kind:     global_buffer
      - .actual_access:  read_only
        .address_space:  global
        .offset:         32
        .size:           8
        .value_kind:     global_buffer
      - .actual_access:  read_only
        .address_space:  global
        .offset:         40
        .size:           8
        .value_kind:     global_buffer
      - .actual_access:  read_only
        .address_space:  global
        .offset:         48
        .size:           8
        .value_kind:     global_buffer
      - .actual_access:  write_only
        .address_space:  global
        .offset:         56
        .size:           8
        .value_kind:     global_buffer
    .group_segment_fixed_size: 16640
    .kernarg_segment_align: 8
    .kernarg_segment_size: 64
    .language:       OpenCL C
    .language_version:
      - 2
      - 0
    .max_flat_workgroup_size: 256
    .name:           _Z11attn_kernelILi4EEvPKfS1_S1_S1_S1_S1_PKcPf
    .private_segment_fixed_size: 0
    .sgpr_count:     38
    .sgpr_spill_count: 0
    .symbol:         _Z11attn_kernelILi4EEvPKfS1_S1_S1_S1_S1_PKcPf.kd
    .uniform_work_group_size: 1
    .uses_dynamic_stack: false
    .vgpr_count:     250
    .vgpr_spill_count: 0
    .wavefront_size: 64
